# s6
# baseline (speedup 1.0000x reference)
_Z11attn_kernelILi4EEvPKfS1_S1_S1_S1_S1_PKcPf:
	s_load_dwordx2 s[24:25], s[0:1], 0x30
	s_load_dwordx8 s[8:15], s[0:1], 0x0
	s_load_dwordx4 s[16:19], s[0:1], 0x20
	v_lshrrev_b32_e32 v63, 6, v0
	v_and_b32_e32 v104, 63, v0
	v_mad_u32_u24 v2, v63, 12, v104
	v_cmp_gt_u32_e32 vcc, 12, v104
	v_and_b32_e32 v57, 15, v0
	v_bfe_u32 v1, v0, 4, 2
	v_cndmask_b32_e32 v2, 48, v2, vcc
	v_lshlrev_b32_e32 v2, 2, v2
	v_lshlrev_b32_e32 v60, 5, v57
	v_lshlrev_b32_e32 v58, 3, v1
	v_add_u32_e32 v3, v60, v58
	v_lshrrev_b32_e32 v56, 4, v0
	v_lshlrev_b32_e32 v54, 4, v57
	v_mov_b32_e32 v59, 0
	s_movk_i32 s4, 0xe0
	v_cmp_gt_u32_e64 s[4:5], s4, v0
	s_lshl_b32 s26, s2, 8
	s_lshl_b32 s27, s2, 9
	s_mul_i32 s28, s2, 14
	v_lshlrev_b32_e32 v5, 2, v57
	v_lshlrev_b32_e32 v147, 9, v57
	s_waitcnt lgkmcnt(0)
	s_add_u32 s20, s24, s26
	s_addc_u32 s21, s25, 0
	s_add_u32 s20, s20, 0x164000
	s_addc_u32 s21, s21, 0
	s_add_u32 s26, s24, s27
	s_addc_u32 s27, s25, 0
	s_add_u32 s26, s26, 0x80000
	s_addc_u32 s27, s27, 0
	global_load_dword v61, v2, s[20:21]
	global_load_dwordx2 v[64:65], v3, s[26:27]
	s_add_u32 s22, s24, 0x160000
	s_addc_u32 s23, s25, 0
	v_cndmask_b32_e64 v62, 13, v56, s[4:5]
	v_add_u32_e32 v3, s28, v62
	v_mad_u32_u24 v144, v3, 36, v5
	v_mad_u32_u24 v146, v3, 12, v5
	v_add_u32_e32 v145, -36, v146
	v_add_u32_e32 v146, -48, v146
	v_lshl_or_b32 v147, v1, 4, v147
	v_lshl_add_u32 v148, v1, 2, v63
	v_min_u32_e32 v148, 13, v148
	v_add_u32_e32 v148, s28, v148
	v_lshl_add_u32 v150, v148, 9, v60
	s_waitcnt vmcnt(1)
	v_readlane_b32 s3, v61, 12
	s_bitcmp0_b32 s3, 1
	s_cselect_b64 s[20:21], -1, 0
	s_cbranch_scc1 .LBB1_16
	v_and_b32_e32 v3, 12, v57
	v_lshlrev_b32_e32 v19, 2, v1
	ds_bpermute_b32 v81, v3, v61
	ds_bpermute_b32 v82, v3, v61 offset:16
	ds_bpermute_b32 v83, v3, v61 offset:32
	ds_bpermute_b32 v84, v19, v61
	ds_bpermute_b32 v85, v19, v61 offset:16
	ds_bpermute_b32 v86, v19, v61 offset:32
	v_and_b32_e32 v87, 3, v57
	v_lshlrev_b32_e32 v87, 4, v87
	v_lshl_or_b32 v87, v1, 6, v87
	v_lshlrev_b32_e32 v88, 3, v57
	s_add_u32 s26, s24, 0x100000
	s_addc_u32 s27, s25, 0
	s_add_u32 s28, s24, 0x140000
	s_addc_u32 s29, s25, 0
	s_waitcnt lgkmcnt(3)
	v_lshl_add_u32 v72, v81, 9, v87
	v_lshl_add_u32 v73, v82, 9, v87
	v_lshl_add_u32 v74, v83, 9, v87
	global_load_dwordx4 v[50:53], v72, s[24:25]
	global_load_dwordx4 v[46:49], v72, s[24:25] offset:256
	global_load_dwordx4 v[14:17], v73, s[24:25]
	global_load_dwordx4 v[10:13], v73, s[24:25] offset:256
	global_load_dwordx4 v[6:9], v74, s[24:25]
	global_load_dwordx4 v[2:5], v74, s[24:25] offset:256
	s_waitcnt lgkmcnt(0)
	v_lshl_add_u32 v75, v84, 8, v54
	v_lshl_add_u32 v78, v84, 7, v88
	v_lshl_add_u32 v76, v85, 8, v54
	v_lshl_add_u32 v79, v85, 7, v88
	v_lshl_add_u32 v77, v86, 8, v54
	v_lshl_add_u32 v80, v86, 7, v88
	global_load_dwordx4 v[30:33], v75, s[26:27]
	global_load_dwordx2 v[70:71], v78, s[28:29]
	global_load_dwordx4 v[26:29], v76, s[26:27]
	global_load_dwordx2 v[66:67], v79, s[28:29]
	global_load_dwordx4 v[18:21], v77, s[26:27]
	global_load_dwordx2 v[68:69], v80, s[28:29]
	s_mov_b32 exec_lo, 0x1ff01ff
	s_mov_b32 exec_hi, 0x1ff01ff
	global_load_dword v120, v144, s[10:11]
	s_mov_b32 exec_lo, 0xe000e00
	s_mov_b32 exec_hi, 0xe000e00
	global_load_dword v120, v145, s[12:13]
	s_mov_b32 exec_lo, 0x70007000
	s_mov_b32 exec_hi, 0x70007000
	global_load_dword v120, v146, s[14:15]
	s_mov_b64 exec, -1
	global_load_dwordx4 v[136:139], v150, s[8:9]
	global_load_dwordx4 v[140:143], v150, s[8:9] offset:16
	s_movk_i32 s6, 0x140
	v_cmp_gt_u32_e32 vcc, s6, v0
	v_lshlrev_b32_e32 v22, 2, v0
	v_mov_b32_e32 v23, 0
	s_and_saveexec_b64 s[6:7], vcc
	ds_write_b32 v22, v23 offset:14336
	s_or_b64 exec, exec, s[6:7]
	v_cmp_gt_u32_e32 vcc, 64, v0
	s_and_saveexec_b64 s[6:7], vcc
	ds_write_b32 v22, v23 offset:15360
	s_or_b64 exec, exec, s[6:7]
	v_bfe_u32 v22, s3, v57, 1
	v_cmp_eq_u32_e32 vcc, 0, v22
	v_mov_b32_e32 v45, 0xc9c35000
	s_mov_b32 s30, 0x3db8aa3b
	s_mov_b32 s31, 0x3db8aa3b
	v_cndmask_b32_e64 v55, 1.0, 0, vcc
	v_mov_b32_e32 v121, 0x3fb8aa3b
	s_bitcmp0_b32 s3, 0
	s_cselect_b64 vcc, -1, 0
	v_cndmask_b32_e32 v34, 0, v45, vcc
	s_bitcmp0_b32 s3, 2
	s_cselect_b64 vcc, -1, 0
	v_cndmask_b32_e32 v36, 0, v45, vcc
	s_bitcmp0_b32 s3, 3
	s_cselect_b64 vcc, -1, 0
	v_cndmask_b32_e32 v37, 0, v45, vcc
	s_bitcmp0_b32 s3, 4
	s_cselect_b64 vcc, -1, 0
	v_cndmask_b32_e32 v22, 0, v45, vcc
	s_bitcmp0_b32 s3, 5
	s_cselect_b64 vcc, -1, 0
	v_cndmask_b32_e32 v23, 0, v45, vcc
	s_bitcmp0_b32 s3, 6
	s_cselect_b64 vcc, -1, 0
	v_cndmask_b32_e32 v24, 0, v45, vcc
	s_bitcmp0_b32 s3, 7
	s_cselect_b64 vcc, -1, 0
	v_cndmask_b32_e32 v25, 0, v45, vcc
	s_bitcmp0_b32 s3, 8
	s_cselect_b64 vcc, -1, 0
	v_cndmask_b32_e32 v38, 0, v45, vcc
	s_bitcmp0_b32 s3, 9
	s_cselect_b64 vcc, -1, 0
	v_cndmask_b32_e32 v39, 0, v45, vcc
	s_bitcmp0_b32 s3, 10
	s_cselect_b64 vcc, -1, 0
	v_cndmask_b32_e32 v40, 0, v45, vcc
	s_bitcmp0_b32 s3, 11
	s_cselect_b64 vcc, -1, 0
	v_cndmask_b32_e32 v41, 0, v45, vcc
	s_bitcmp0_b32 s3, 12
	s_cselect_b64 vcc, -1, 0
	v_cndmask_b32_e32 v42, 0, v45, vcc
	s_bitcmp0_b32 s3, 13
	s_cselect_b64 vcc, -1, 0
	v_cndmask_b32_e32 v43, 0, v45, vcc
	v_mov_b32_e32 v35, 0
	v_mov_b32_e32 v44, v45
	v_mov_b32_e32 v75, 0
	v_mov_b32_e32 v79, 0
	v_mov_b32_e32 v83, 0
	s_waitcnt vmcnt(16)
	v_mfma_f32_16x16x32_fp8_fp8 v[160:163], v[50:51], v[64:65], v[34:37]
	v_mfma_f32_16x16x32_fp8_fp8 v[164:167], v[52:53], v[64:65], v[22:25]
	s_waitcnt vmcnt(15)
	v_mfma_f32_16x16x32_fp8_fp8 v[168:171], v[46:47], v[64:65], v[38:41]
	v_mfma_f32_16x16x32_fp8_fp8 v[172:175], v[48:49], v[64:65], v[42:45]
	s_nop 3
	v_max3_f32 v86, v160, v161, v162
	v_max3_f32 v87, v163, v164, v165
	v_max3_f32 v88, v166, v167, v168
	v_max3_f32 v89, v169, v170, v171
	v_max3_f32 v86, v86, v172, v173
	v_max3_f32 v87, v87, v88, v89
	v_max_f32_e32 v96, v86, v87
	v_mul_f32_e32 v98, 0xbdb8aa3b, v96
	v_pk_fma_f32 v[208:209], v[160:161], s[30:31], v[98:99] op_sel_hi:[1,1,0]
	v_pk_fma_f32 v[210:211], v[162:163], s[30:31], v[98:99] op_sel_hi:[1,1,0]
	v_pk_fma_f32 v[212:213], v[164:165], s[30:31], v[98:99] op_sel_hi:[1,1,0]
	v_pk_fma_f32 v[214:215], v[166:167], s[30:31], v[98:99] op_sel_hi:[1,1,0]
	v_pk_fma_f32 v[216:217], v[168:169], s[30:31], v[98:99] op_sel_hi:[1,1,0]
	v_pk_fma_f32 v[218:219], v[170:171], s[30:31], v[98:99] op_sel_hi:[1,1,0]
	v_pk_fma_f32 v[220:221], v[172:173], s[30:31], v[98:99] op_sel_hi:[1,1,0]
	v_exp_f32_e32 v208, v208
	v_exp_f32_e32 v209, v209
	v_exp_f32_e32 v210, v210
	v_exp_f32_e32 v211, v211
	v_exp_f32_e32 v212, v212
	v_exp_f32_e32 v213, v213
	v_exp_f32_e32 v214, v214
	v_exp_f32_e32 v215, v215
	v_exp_f32_e32 v216, v216
	v_exp_f32_e32 v217, v217
	v_exp_f32_e32 v218, v218
	v_exp_f32_e32 v219, v219
	v_exp_f32_e32 v220, v220
	v_exp_f32_e32 v221, v221
	s_waitcnt vmcnt(14)
	v_mfma_f32_16x16x32_fp8_fp8 v[176:179], v[14:15], v[64:65], v[34:37]
	v_mfma_f32_16x16x32_fp8_fp8 v[180:183], v[16:17], v[64:65], v[22:25]
	s_waitcnt vmcnt(13)
	v_mfma_f32_16x16x32_fp8_fp8 v[184:187], v[10:11], v[64:65], v[38:41]
	v_mfma_f32_16x16x32_fp8_fp8 v[188:191], v[12:13], v[64:65], v[42:45]
	v_pk_add_f32 v[86:87], v[208:209], v[210:211]
	v_pk_add_f32 v[88:89], v[212:213], v[214:215]
	v_pk_add_f32 v[90:91], v[216:217], v[218:219]
	v_pk_mul_f32 v[92:93], v[208:209], v[160:161]
	v_pk_mul_f32 v[94:95], v[210:211], v[162:163]
	v_pk_add_f32 v[86:87], v[86:87], v[220:221]
	v_pk_add_f32 v[88:89], v[88:89], v[90:91]
	v_pk_fma_f32 v[92:93], v[212:213], v[164:165], v[92:93]
	v_pk_fma_f32 v[94:95], v[214:215], v[166:167], v[94:95]
	v_pk_add_f32 v[86:87], v[86:87], v[88:89]
	v_pk_fma_f32 v[92:93], v[216:217], v[168:169], v[92:93]
	v_pk_fma_f32 v[94:95], v[218:219], v[170:171], v[94:95]
	v_add_f32_e32 v86, v86, v87
	v_pk_fma_f32 v[92:93], v[220:221], v[172:173], v[92:93]
	v_rcp_f32_e32 v87, v86
	v_pk_add_f32 v[92:93], v[92:93], v[94:95]
	v_mul_f32_e32 v87, v55, v87
	v_add_f32_e32 v92, v92, v93
	v_mul_f32_e32 v107, v86, v87
	v_mul_f32_e32 v92, v92, v87
	v_mul_f32_e32 v100, 0x43800000, v87
	v_mul_f32_e32 v103, 0x3d800000, v92
	v_max3_f32 v86, v176, v177, v178
	v_max3_f32 v87, v179, v180, v181
	v_max3_f32 v88, v182, v183, v184
	v_max3_f32 v89, v185, v186, v187
	v_max3_f32 v86, v86, v188, v189
	v_max3_f32 v87, v87, v88, v89
	v_max_f32_e32 v96, v86, v87
	v_mul_f32_e32 v98, 0xbdb8aa3b, v96
	v_pk_fma_f32 v[222:223], v[176:177], s[30:31], v[98:99] op_sel_hi:[1,1,0]
	v_pk_fma_f32 v[224:225], v[178:179], s[30:31], v[98:99] op_sel_hi:[1,1,0]
	v_pk_fma_f32 v[226:227], v[180:181], s[30:31], v[98:99] op_sel_hi:[1,1,0]
	v_pk_fma_f32 v[228:229], v[182:183], s[30:31], v[98:99] op_sel_hi:[1,1,0]
	v_pk_fma_f32 v[230:231], v[184:185], s[30:31], v[98:99] op_sel_hi:[1,1,0]
	v_pk_fma_f32 v[232:233], v[186:187], s[30:31], v[98:99] op_sel_hi:[1,1,0]
	v_pk_fma_f32 v[234:235], v[188:189], s[30:31], v[98:99] op_sel_hi:[1,1,0]
	v_exp_f32_e32 v222, v222
	v_exp_f32_e32 v223, v223
	v_exp_f32_e32 v224, v224
	v_exp_f32_e32 v225, v225
	v_exp_f32_e32 v226, v226
	v_exp_f32_e32 v227, v227
	v_exp_f32_e32 v228, v228
	v_exp_f32_e32 v229, v229
	v_exp_f32_e32 v230, v230
	v_exp_f32_e32 v231, v231
	v_exp_f32_e32 v232, v232
	v_exp_f32_e32 v233, v233
	v_exp_f32_e32 v234, v234
	v_exp_f32_e32 v235, v235
	s_waitcnt vmcnt(12)
	v_mfma_f32_16x16x32_fp8_fp8 v[192:195], v[6:7], v[64:65], v[34:37]
	v_mfma_f32_16x16x32_fp8_fp8 v[196:199], v[8:9], v[64:65], v[22:25]
	s_waitcnt vmcnt(11)
	v_mfma_f32_16x16x32_fp8_fp8 v[200:203], v[2:3], v[64:65], v[38:41]
	v_mfma_f32_16x16x32_fp8_fp8 v[204:207], v[4:5], v[64:65], v[42:45]
	v_pk_add_f32 v[86:87], v[222:223], v[224:225]
	v_pk_add_f32 v[88:89], v[226:227], v[228:229]
	v_pk_add_f32 v[90:91], v[230:231], v[232:233]
	v_pk_mul_f32 v[92:93], v[222:223], v[176:177]
	v_pk_mul_f32 v[94:95], v[224:225], v[178:179]
	v_pk_add_f32 v[86:87], v[86:87], v[234:235]
	v_pk_add_f32 v[88:89], v[88:89], v[90:91]
	v_pk_fma_f32 v[92:93], v[226:227], v[180:181], v[92:93]
	v_pk_fma_f32 v[94:95], v[228:229], v[182:183], v[94:95]
	v_pk_add_f32 v[86:87], v[86:87], v[88:89]
	v_pk_fma_f32 v[92:93], v[230:231], v[184:185], v[92:93]
	v_pk_fma_f32 v[94:95], v[232:233], v[186:187], v[94:95]
	v_add_f32_e32 v86, v86, v87
	v_pk_fma_f32 v[92:93], v[234:235], v[188:189], v[92:93]
	v_rcp_f32_e32 v87, v86
	v_pk_add_f32 v[92:93], v[92:93], v[94:95]
	v_mul_f32_e32 v87, v55, v87
	v_add_f32_e32 v92, v92, v93
	v_mul_f32_e32 v108, v86, v87
	v_mul_f32_e32 v92, v92, v87
	v_mul_f32_e32 v101, 0x43800000, v87
	v_mul_f32_e32 v105, 0x3d800000, v92
	v_max3_f32 v86, v192, v193, v194
	v_max3_f32 v87, v195, v196, v197
	v_max3_f32 v88, v198, v199, v200
	v_max3_f32 v89, v201, v202, v203
	v_max3_f32 v86, v86, v204, v205
	v_max3_f32 v87, v87, v88, v89
	v_max_f32_e32 v96, v86, v87
	v_mul_f32_e32 v98, 0xbdb8aa3b, v96
	v_pk_fma_f32 v[236:237], v[192:193], s[30:31], v[98:99] op_sel_hi:[1,1,0]
	v_pk_fma_f32 v[238:239], v[194:195], s[30:31], v[98:99] op_sel_hi:[1,1,0]
	v_pk_fma_f32 v[240:241], v[196:197], s[30:31], v[98:99] op_sel_hi:[1,1,0]
	v_pk_fma_f32 v[242:243], v[198:199], s[30:31], v[98:99] op_sel_hi:[1,1,0]
	v_pk_fma_f32 v[244:245], v[200:201], s[30:31], v[98:99] op_sel_hi:[1,1,0]
	v_pk_fma_f32 v[246:247], v[202:203], s[30:31], v[98:99] op_sel_hi:[1,1,0]
	v_pk_fma_f32 v[248:249], v[204:205], s[30:31], v[98:99] op_sel_hi:[1,1,0]
	v_exp_f32_e32 v236, v236
	v_exp_f32_e32 v237, v237
	v_exp_f32_e32 v238, v238
	v_exp_f32_e32 v239, v239
	v_exp_f32_e32 v240, v240
	v_exp_f32_e32 v241, v241
	v_exp_f32_e32 v242, v242
	v_exp_f32_e32 v243, v243
	v_exp_f32_e32 v244, v244
	v_exp_f32_e32 v245, v245
	v_exp_f32_e32 v246, v246
	v_exp_f32_e32 v247, v247
	v_exp_f32_e32 v248, v248
	v_exp_f32_e32 v249, v249
	v_pk_add_f32 v[86:87], v[236:237], v[238:239]
	v_pk_add_f32 v[88:89], v[240:241], v[242:243]
	v_pk_add_f32 v[90:91], v[244:245], v[246:247]
	v_pk_mul_f32 v[92:93], v[236:237], v[192:193]
	v_pk_mul_f32 v[94:95], v[238:239], v[194:195]
	v_pk_add_f32 v[86:87], v[86:87], v[248:249]
	v_pk_add_f32 v[88:89], v[88:89], v[90:91]
	v_pk_fma_f32 v[92:93], v[240:241], v[196:197], v[92:93]
	v_pk_fma_f32 v[94:95], v[242:243], v[198:199], v[94:95]
	v_pk_add_f32 v[86:87], v[86:87], v[88:89]
	v_pk_fma_f32 v[92:93], v[244:245], v[200:201], v[92:93]
	v_pk_fma_f32 v[94:95], v[246:247], v[202:203], v[94:95]
	v_add_f32_e32 v86, v86, v87
	v_pk_fma_f32 v[92:93], v[248:249], v[204:205], v[92:93]
	v_rcp_f32_e32 v87, v86
	v_pk_add_f32 v[92:93], v[92:93], v[94:95]
	v_mul_f32_e32 v87, v55, v87
	v_add_f32_e32 v92, v92, v93
	v_mul_f32_e32 v109, v86, v87
	v_mul_f32_e32 v92, v92, v87
	v_mul_f32_e32 v102, 0x43800000, v87
	v_mul_f32_e32 v106, 0x3d800000, v92
	v_max3_f32 v122, v103, v105, v106
	v_cmp_gt_u32_e64 s[6:7], 16, v104
	v_mov_b32_e32 v123, v122
	s_nop 1
	v_permlane16_swap_b32_e32 v122, v123
	v_max_f32_e32 v122, v122, v123
	v_mov_b32_e32 v123, v122
	s_nop 1
	v_permlane32_swap_b32_e32 v122, v123
	v_max_f32_e32 v36, v122, v123
	v_mul_f32_e32 v123, 0x3fb8aa3b, v36
	v_fma_f32 v111, v103, v121, -v123
	v_exp_f32_e32 v111, v111
	s_nop 0
	v_mul_f32_e32 v112, v111, v100
	v_mul_f32_e32 v110, v111, v107
	v_mov_b32_e32 v114, v111
	v_pk_mul_f32 v[208:209], v[208:209], v[112:113] op_sel_hi:[1,0]
	v_pk_mul_f32 v[210:211], v[210:211], v[112:113] op_sel_hi:[1,0]
	v_pk_mul_f32 v[212:213], v[212:213], v[112:113] op_sel_hi:[1,0]
	v_pk_mul_f32 v[214:215], v[214:215], v[112:113] op_sel_hi:[1,0]
	v_pk_mul_f32 v[216:217], v[216:217], v[112:113] op_sel_hi:[1,0]
	v_pk_mul_f32 v[218:219], v[218:219], v[112:113] op_sel_hi:[1,0]
	v_pk_mul_f32 v[220:221], v[220:221], v[112:113] op_sel_hi:[1,0]
	s_waitcnt vmcnt(9)
	v_mov_b32_e32 v115, v110
	v_fma_mix_f32 v116, v110, v70, 0 op_sel_hi:[0,1,0]
	v_fma_mix_f32 v117, v110, v70, 0 op_sel:[0,1,0] op_sel_hi:[0,1,0]
	v_fma_mix_f32 v118, v110, v71, 0 op_sel_hi:[0,1,0]
	v_cvt_pk_fp8_f32 v72, v208, v209
	v_cvt_pk_fp8_f32 v73, v212, v213
	v_cvt_pk_fp8_f32 v74, v216, v217
	v_cvt_pk_fp8_f32 v75, v220, v221
	v_cvt_pk_fp8_f32 v72, v210, v211 op_sel:[0,0,1]
	v_cvt_pk_fp8_f32 v73, v214, v215 op_sel:[0,0,1]
	v_cvt_pk_fp8_f32 v74, v218, v219 op_sel:[0,0,1]
	s_nop 1
	v_mfma_f32_16x16x32_fp8_fp8 v[152:155], v[72:73], v[30:31], 0
	v_mfma_f32_16x16x32_fp8_fp8 v[152:155], v[74:75], v[32:33], v[152:155]
	v_fma_f32 v111, v105, v121, -v123
	v_exp_f32_e32 v111, v111
	s_nop 0
	v_mul_f32_e32 v112, v111, v101
	v_mul_f32_e32 v110, v111, v108
	v_add_f32_e32 v114, v114, v111
	v_pk_mul_f32 v[222:223], v[222:223], v[112:113] op_sel_hi:[1,0]
	v_pk_mul_f32 v[224:225], v[224:225], v[112:113] op_sel_hi:[1,0]
	v_pk_mul_f32 v[226:227], v[226:227], v[112:113] op_sel_hi:[1,0]
	v_pk_mul_f32 v[228:229], v[228:229], v[112:113] op_sel_hi:[1,0]
	v_pk_mul_f32 v[230:231], v[230:231], v[112:113] op_sel_hi:[1,0]
	v_pk_mul_f32 v[232:233], v[232:233], v[112:113] op_sel_hi:[1,0]
	v_pk_mul_f32 v[234:235], v[234:235], v[112:113] op_sel_hi:[1,0]
	s_waitcnt vmcnt(7)
	v_add_f32_e32 v115, v115, v110
	v_fma_mix_f32 v116, v110, v66, v116 op_sel_hi:[0,1,0]
	v_fma_mix_f32 v117, v110, v66, v117 op_sel:[0,1,0] op_sel_hi:[0,1,0]
	v_fma_mix_f32 v118, v110, v67, v118 op_sel_hi:[0,1,0]
	v_cvt_pk_fp8_f32 v76, v222, v223
	v_cvt_pk_fp8_f32 v77, v226, v227
	v_cvt_pk_fp8_f32 v78, v230, v231
	v_cvt_pk_fp8_f32 v79, v234, v235
	v_cvt_pk_fp8_f32 v76, v224, v225 op_sel:[0,0,1]
	v_cvt_pk_fp8_f32 v77, v228, v229 op_sel:[0,0,1]
	v_cvt_pk_fp8_f32 v78, v232, v233 op_sel:[0,0,1]
	s_nop 1
	v_mfma_f32_16x16x32_fp8_fp8 v[152:155], v[76:77], v[26:27], v[152:155]
	v_mfma_f32_16x16x32_fp8_fp8 v[152:155], v[78:79], v[28:29], v[152:155]
	v_fma_f32 v111, v106, v121, -v123
	v_exp_f32_e32 v111, v111
	s_nop 0
	v_mul_f32_e32 v112, v111, v102
	v_mul_f32_e32 v110, v111, v109
	v_add_f32_e32 v114, v114, v111
	v_pk_mul_f32 v[236:237], v[236:237], v[112:113] op_sel_hi:[1,0]
	v_pk_mul_f32 v[238:239], v[238:239], v[112:113] op_sel_hi:[1,0]
	v_pk_mul_f32 v[240:241], v[240:241], v[112:113] op_sel_hi:[1,0]
	v_pk_mul_f32 v[242:243], v[242:243], v[112:113] op_sel_hi:[1,0]
	v_pk_mul_f32 v[244:245], v[244:245], v[112:113] op_sel_hi:[1,0]
	v_pk_mul_f32 v[246:247], v[246:247], v[112:113] op_sel_hi:[1,0]
	v_pk_mul_f32 v[248:249], v[248:249], v[112:113] op_sel_hi:[1,0]
	s_waitcnt vmcnt(5)
	v_add_f32_e32 v115, v115, v110
	v_fma_mix_f32 v116, v110, v68, v116 op_sel_hi:[0,1,0]
	v_fma_mix_f32 v117, v110, v68, v117 op_sel:[0,1,0] op_sel_hi:[0,1,0]
	v_fma_mix_f32 v118, v110, v69, v118 op_sel_hi:[0,1,0]
	v_cvt_pk_fp8_f32 v80, v236, v237
	v_cvt_pk_fp8_f32 v81, v240, v241
	v_cvt_pk_fp8_f32 v82, v244, v245
	v_cvt_pk_fp8_f32 v83, v248, v249
	v_cvt_pk_fp8_f32 v80, v238, v239 op_sel:[0,0,1]
	v_cvt_pk_fp8_f32 v81, v242, v243 op_sel:[0,0,1]
	v_cvt_pk_fp8_f32 v82, v246, v247 op_sel:[0,0,1]
	s_nop 1
	v_mfma_f32_16x16x32_fp8_fp8 v[152:155], v[80:81], v[18:19], v[152:155]
	v_mfma_f32_16x16x32_fp8_fp8 v[152:155], v[82:83], v[20:21], v[152:155]
	v_mov_b32_e32 v86, v114
	v_mov_b32_e32 v87, v115
	v_mov_b32_e32 v88, v116
	v_mov_b32_e32 v89, v117
	v_mov_b32_e32 v90, v118
	v_permlane16_swap_b32_e32 v114, v86
	v_permlane16_swap_b32_e32 v115, v87
	v_permlane16_swap_b32_e32 v116, v88
	v_permlane16_swap_b32_e32 v117, v89
	v_permlane16_swap_b32_e32 v118, v90
	v_add_f32_e32 v114, v114, v86
	v_add_f32_e32 v115, v115, v87
	v_add_f32_e32 v116, v116, v88
	v_add_f32_e32 v117, v117, v89
	v_add_f32_e32 v118, v118, v90
	v_mov_b32_e32 v86, v114
	v_mov_b32_e32 v87, v115
	v_mov_b32_e32 v88, v116
	v_mov_b32_e32 v89, v117
	v_mov_b32_e32 v90, v118
	v_permlane32_swap_b32_e32 v114, v86
	v_permlane32_swap_b32_e32 v115, v87
	v_permlane32_swap_b32_e32 v116, v88
	v_permlane32_swap_b32_e32 v117, v89
	v_permlane32_swap_b32_e32 v118, v90
	v_mul_u32_u24_e32 v91, 0x140, v1
	s_movk_i32 s26, 0x500
	v_mad_u32_u24 v91, v63, s26, v91
	v_lshl_or_b32 v91, v57, 2, v91
	v_add_u32_e32 v91, 0x1c00, v91
	v_add_f32_e32 v37, v114, v86
	v_add_f32_e32 v20, v115, v87
	v_add_f32_e32 v18, v116, v88
	v_add_f32_e32 v19, v117, v89
	v_add_f32_e32 v21, v118, v90
	ds_write2_b32 v91, v152, v153 offset0:0 offset1:20
	ds_write2_b32 v91, v154, v155 offset0:40 offset1:60
	s_branch .LBB1_30
.LBB1_16:
	s_mov_b32 exec_lo, 0x1ff01ff
	s_mov_b32 exec_hi, 0x1ff01ff
	global_load_dword v120, v144, s[10:11]
	s_mov_b32 exec_lo, 0xe000e00
	s_mov_b32 exec_hi, 0xe000e00
	global_load_dword v120, v145, s[12:13]
	s_mov_b32 exec_lo, 0x70007000
	s_mov_b32 exec_hi, 0x70007000
	global_load_dword v120, v146, s[14:15]
	s_mov_b64 exec, -1
	global_load_dwordx4 v[136:139], v150, s[8:9]
	global_load_dwordx4 v[140:143], v150, s[8:9] offset:16
	s_movk_i32 s6, 0x140
	v_cmp_gt_u32_e32 vcc, s6, v0
	v_lshlrev_b32_e32 v18, 2, v0
	v_mov_b32_e32 v19, 0
	s_and_saveexec_b64 s[6:7], vcc
	ds_write_b32 v18, v19 offset:14336
	s_or_b64 exec, exec, s[6:7]
	v_cmp_gt_u32_e32 vcc, 64, v0
	s_and_saveexec_b64 s[6:7], vcc
	ds_write_b32 v18, v19 offset:15360
	s_or_b64 exec, exec, s[6:7]
	v_mul_u32_u24_e32 v18, 0x140, v1
	s_movk_i32 s6, 0x500
	v_mad_u32_u24 v18, v63, s6, v18
	v_lshl_or_b32 v18, v57, 2, v18
	v_mov_b32_e32 v21, 0
	v_add_u32_e32 v18, 0x1c00, v18
	ds_write2_b32 v18, v21, v21 offset1:20
	ds_write2_b32 v18, v21, v21 offset0:40 offset1:60
	v_cmp_gt_u32_e64 s[6:7], 16, v104
	v_mov_b32_e32 v37, 1.0
	v_mov_b32_e32 v20, 0
	v_mov_b32_e32 v19, 0
	v_mov_b32_e32 v18, 0
	v_mov_b32_e32 v36, 0
.LBB1_30:
	global_load_dwordx4 v[160:163], v147, s[22:23]
	global_load_dwordx4 v[164:167], v147, s[22:23] offset:64
	global_load_dwordx4 v[168:171], v147, s[22:23] offset:128
	global_load_dwordx4 v[172:175], v147, s[22:23] offset:192
	global_load_dwordx4 v[176:179], v147, s[22:23] offset:256
	global_load_dwordx4 v[180:183], v147, s[22:23] offset:320
	global_load_dwordx4 v[184:187], v147, s[22:23] offset:384
	global_load_dwordx4 v[188:191], v147, s[22:23] offset:448
	global_load_dwordx4 v[192:195], v60, s[16:17]
	global_load_dwordx4 v[196:199], v60, s[16:17] offset:16
	global_load_dwordx4 v[200:203], v60, s[18:19]
	global_load_dwordx4 v[204:207], v60, s[18:19] offset:16
	s_waitcnt lgkmcnt(0)
	s_and_saveexec_b64 s[8:9], s[6:7]
	s_cbranch_execz .LBB1_32
	v_mov_b32_e32 v39, 0
	v_lshl_or_b32 v26, v63, 9, v60
	v_mov_b32_e32 v38, v20
	v_mov_b32_e32 v20, v21
	v_mov_b32_e32 v21, v39
	ds_write_b128 v26, v[36:39] offset:12288
	ds_write_b128 v26, v[18:21] offset:12304

.LBB1_36:
	s_or_b64 exec, exec, s[10:11]
	v_fma_f32 v34, v21, v36, 0
	s_waitcnt lgkmcnt(1)
	v_fma_f32 v35, v21, v38, 0
	v_fmac_f32_e32 v34, v29, v28
	v_fmac_f32_e32 v35, v29, v39
	v_fmac_f32_e32 v34, v30, v32
	s_waitcnt lgkmcnt(0)
	v_fmac_f32_e32 v35, v30, v26
	v_fmac_f32_e32 v34, v33, v20
	v_fmac_f32_e32 v35, v33, v27
	s_waitcnt vmcnt(14)
	v_mov_b32_dpp v33, v120 row_newbcast:10 row_mask:0xf bank_mask:0xf bound_ctrl:1
	v_mov_b32_dpp v36, v120 row_newbcast:11 row_mask:0xf bank_mask:0xf bound_ctrl:1
	v_cmp_eq_u32_e64 s[10:11], 1, v57
	v_mov_b32_dpp v32, v120 row_newbcast:9 row_mask:0xf bank_mask:0xf bound_ctrl:1
	v_mov_b32_dpp v38, v120 row_newbcast:13 row_mask:0xf bank_mask:0xf bound_ctrl:1
	v_mov_b32_dpp v39, v120 row_newbcast:14 row_mask:0xf bank_mask:0xf bound_ctrl:1
	v_cndmask_b32_e64 v33, v36, v33, s[10:11]
	v_cmp_eq_u32_e64 s[8:9], 0, v57
	v_mov_b32_dpp v37, v120 row_newbcast:12 row_mask:0xf bank_mask:0xf bound_ctrl:1
	v_mov_b32_dpp v27, v120 row_newbcast:0 row_mask:0xf bank_mask:0xf bound_ctrl:1
	v_cndmask_b32_e64 v32, v33, v32, s[8:9]
	v_cndmask_b32_e64 v33, v39, v38, s[10:11]
	v_cndmask_b32_e64 v33, v33, v37, s[8:9]
	v_fma_f32 v33, v34, v33, -v35
	v_fma_f32 v32, v18, v33, -v32
	v_mov_b32_dpp v20, v120 row_newbcast:1 row_mask:0xf bank_mask:0xf bound_ctrl:1
	v_mov_b32_dpp v19, v120 row_newbcast:2 row_mask:0xf bank_mask:0xf bound_ctrl:1
	v_mov_b32_dpp v31, v120 row_newbcast:3 row_mask:0xf bank_mask:0xf bound_ctrl:1
	v_mov_b32_dpp v29, v120 row_newbcast:4 row_mask:0xf bank_mask:0xf bound_ctrl:1
	v_mov_b32_dpp v26, v120 row_newbcast:5 row_mask:0xf bank_mask:0xf bound_ctrl:1
	v_mov_b32_dpp v30, v120 row_newbcast:6 row_mask:0xf bank_mask:0xf bound_ctrl:1
	v_mov_b32_dpp v28, v120 row_newbcast:7 row_mask:0xf bank_mask:0xf bound_ctrl:1
	v_mov_b32_dpp v21, v120 row_newbcast:8 row_mask:0xf bank_mask:0xf bound_ctrl:1
	v_mov_b32_dpp v18, v32 quad_perm:[0,0,0,0] row_mask:0xf bank_mask:0xf bound_ctrl:1
	v_mov_b32_dpp v33, v32 quad_perm:[1,1,1,1] row_mask:0xf bank_mask:0xf bound_ctrl:1
	v_mov_b32_dpp v32, v32 quad_perm:[2,2,2,2] row_mask:0xf bank_mask:0xf bound_ctrl:1
	s_and_b64 s[12:13], vcc, s[4:5]
	s_and_b64 exec, exec, s[12:13]
	s_cbranch_execz .LBB1_39
	v_mul_f32_e32 v31, v31, v33
	v_fmac_f32_e32 v31, v27, v18
	v_mul_f32_e32 v27, v29, v33
	v_fmac_f32_e32 v27, v20, v18
	v_fmac_f32_e32 v27, v28, v32
	v_mul_f32_e32 v20, v26, v33
	v_fmac_f32_e32 v31, v30, v32
	v_fmac_f32_e32 v20, v19, v18
	v_mul_f32_e32 v18, v27, v27
	v_fmac_f32_e32 v20, v21, v32
	v_fmac_f32_e32 v18, v31, v31
	v_fmac_f32_e32 v18, v20, v20
	v_mad_u32_u24 v26, v56, 3, v57
	v_sqrt_f32_e32 v18, v18
	v_cndmask_b32_e64 v19, v20, v27, s[10:11]
	v_add_u32_e32 v29, 56, v26
	v_add_f32_e32 v21, 0x38d1b717, v18
	v_rcp_f32_e32 v21, v21
	v_cndmask_b32_e64 v20, v19, v31, s[8:9]
	v_mul_u32_u24_e32 v28, 0x2493, v26
	v_mul_u32_u24_e32 v30, 0x2493, v29
	v_lshrrev_b32_e32 v28, 16, v28
	v_lshrrev_b32_e32 v30, 16, v30
	v_mul_u32_u24_e32 v28, 66, v28
	v_mul_u32_u24_e32 v30, 66, v30
	v_lshl_add_u32 v28, v26, 1, v28
	v_lshl_add_u32 v30, v29, 1, v30
	v_cvt_f16_f32_e32 v27, v20
	v_fma_mixlo_f16 v20, v20, v21, 0
	ds_write_b16 v28, v27 offset:14368
	ds_write_b16 v30, v20 offset:14368
	s_and_b64 exec, exec, s[8:9]
	s_cbranch_execz .LBB1_39
	v_cmp_lt_u32_e32 vcc, 6, v56
	v_cvt_f16_f32_e32 v18, v18
	v_lshlrev_b32_e32 v19, 1, v56
	v_mov_b32_e32 v20, 0x42
	v_cndmask_b32_e32 v20, 0, v20, vcc
	v_add_u32_e32 v19, v19, v20
	ds_write_b16 v19, v18 offset:14848
.LBB1_39:
	s_or_b64 exec, exec, s[14:15]
	s_load_dwordx2 s[14:15], s[0:1], 0x38
	v_add_u32_e32 v18, v57, v63
	v_and_b32_e32 v18, 3, v18
	v_and_or_b32 v18, v57, 12, v18
	v_mul_u32_u24_e32 v18, 0x50, v18
	v_lshl_add_u32 v18, v1, 4, v18
	v_lshl_add_u32 v22, v1, 2, v63
	v_lshrrev_b32_e64 v23, v22, s3
	v_and_b32_e32 v23, 1, v23
	v_cvt_f32_u32_e32 v23, v23
	s_waitcnt lgkmcnt(0)
	s_barrier
	ds_read_b128 v[18:21], v18 offset:14336
	s_waitcnt vmcnt(4) lgkmcnt(0)
	v_mfma_f32_16x16x32_f16 v[208:211], v[18:21], v[160:163], 0
	v_mfma_f32_16x16x32_f16 v[212:215], v[18:21], v[164:167], 0
	v_mfma_f32_16x16x32_f16 v[216:219], v[18:21], v[168:171], 0
	v_mfma_f32_16x16x32_f16 v[220:223], v[18:21], v[172:175], 0
	v_mfma_f32_16x16x32_f16 v[224:227], v[18:21], v[176:179], 0
	v_mfma_f32_16x16x32_f16 v[228:231], v[18:21], v[180:183], 0
	v_mfma_f32_16x16x32_f16 v[232:235], v[18:21], v[184:187], 0
	v_mfma_f32_16x16x32_f16 v[236:239], v[18:21], v[188:191], 0
	s_nop 0
	v_fma_f32 v136, v208, v23, v136
	v_fma_f32 v137, v212, v23, v137
	v_fma_f32 v138, v216, v23, v138
	v_fma_f32 v139, v220, v23, v139
	v_fma_f32 v140, v224, v23, v140
	v_fma_f32 v141, v228, v23, v141
	v_fma_f32 v142, v232, v23, v142
	v_fma_f32 v143, v236, v23, v143
	v_pk_add_f32 v[24:25], v[136:137], v[138:139]
	v_pk_add_f32 v[26:27], v[140:141], v[142:143]
	v_cmp_gt_u32_e32 vcc, 14, v22
	v_pk_add_f32 v[24:25], v[24:25], v[26:27]
	s_nop 0
	v_add_f32_e32 v24, v24, v25
	s_nop 1
	v_add_f32_dpp v24, v24, v24 quad_perm:[1,0,3,2] row_mask:0xf bank_mask:0xf bound_ctrl:1
	s_nop 1
	v_add_f32_dpp v24, v24, v24 quad_perm:[2,3,0,1] row_mask:0xf bank_mask:0xf bound_ctrl:1
	s_nop 1
	v_add_f32_dpp v24, v24, v24 row_half_mirror row_mask:0xf bank_mask:0xf bound_ctrl:1
	s_nop 1
	v_add_f32_dpp v24, v24, v24 row_mirror row_mask:0xf bank_mask:0xf bound_ctrl:1
	v_mul_f32_e32 v24, 0x3c000000, v24
	v_pk_add_f32 v[136:137], v[136:137], v[24:25] op_sel_hi:[1,0] neg_lo:[0,1] neg_hi:[0,1]
	v_pk_add_f32 v[138:139], v[138:139], v[24:25] op_sel_hi:[1,0] neg_lo:[0,1] neg_hi:[0,1]
	v_pk_add_f32 v[140:141], v[140:141], v[24:25] op_sel_hi:[1,0] neg_lo:[0,1] neg_hi:[0,1]
	v_pk_add_f32 v[142:143], v[142:143], v[24:25] op_sel_hi:[1,0] neg_lo:[0,1] neg_hi:[0,1]
	v_pk_mul_f32 v[26:27], v[136:137], v[136:137]
	v_pk_mul_f32 v[28:29], v[138:139], v[138:139]
	v_pk_fma_f32 v[26:27], v[140:141], v[140:141], v[26:27]
	v_pk_fma_f32 v[28:29], v[142:143], v[142:143], v[28:29]
	v_mov_b32_e32 v25, 0x3727c5ac
	v_pk_add_f32 v[26:27], v[26:27], v[28:29]
	s_nop 0
	v_add_f32_e32 v26, v26, v27
	s_nop 1
	v_add_f32_dpp v26, v26, v26 quad_perm:[1,0,3,2] row_mask:0xf bank_mask:0xf bound_ctrl:1
	s_nop 1
	v_add_f32_dpp v26, v26, v26 quad_perm:[2,3,0,1] row_mask:0xf bank_mask:0xf bound_ctrl:1
	s_nop 1
	v_add_f32_dpp v26, v26, v26 row_half_mirror row_mask:0xf bank_mask:0xf bound_ctrl:1
	s_nop 1
	v_add_f32_dpp v26, v26, v26 row_mirror row_mask:0xf bank_mask:0xf bound_ctrl:1
	v_fmac_f32_e32 v25, 0x3c000000, v26
	v_rsq_f32_e32 v24, v25
	s_nop 0
	v_pk_mul_f32 v[136:137], v[136:137], v[24:25] op_sel_hi:[1,0]
	v_pk_mul_f32 v[138:139], v[138:139], v[24:25] op_sel_hi:[1,0]
	v_pk_mul_f32 v[140:141], v[140:141], v[24:25] op_sel_hi:[1,0]
	v_pk_mul_f32 v[142:143], v[142:143], v[24:25] op_sel_hi:[1,0]
	s_waitcnt vmcnt(0)
	v_pk_fma_f32 v[136:137], v[192:193], v[136:137], v[200:201]
	v_pk_fma_f32 v[138:139], v[194:195], v[138:139], v[202:203]
	v_pk_fma_f32 v[140:141], v[196:197], v[140:141], v[204:205]
	v_pk_fma_f32 v[142:143], v[198:199], v[142:143], v[206:207]
	s_and_saveexec_b64 s[0:1], vcc
	global_store_dwordx4 v150, v[136:139], s[14:15] nt
	global_store_dwordx4 v150, v[140:143], s[14:15] offset:16 nt
	s_endpgm
